# v19: v17 + P2 max|k| scan keeps 8 row pairs in flight (unrolled)
# speedup vs baseline: 1.0028x; 1.0028x over previous
; template <int PH>
; __device__ __forceinline__ void mk_body(const Args& a) {
;     ...
;         for (int blk = gw; blk < M / 32; blk += ngw) {
;             float mx2 = 0.f;
;             for (int i = 0; i < 32; ++i) {
;                 const u32x4 v = *(const u32x4*)(y0 + (size_t)(blk * 32 + i) * Y0P + Y0_FK + 8 * lane);
;                 float s = 0.f;
; #pragma unroll
;                 for (int j = 0; j < 4; ++j) { const float lo_ = __uint_as_float(v[j] << 16), hi_ = __uint_as_float(v[j] & 0xffff0000u); s = fmaf(lo_, lo_, s); s = fmaf(hi_, hi_, s); }
;                 s += __shfl_xor(s, 1); s += __shfl_xor(s, 2); s += __shfl_xor(s, 4);
;                 mx2 = fmaxf(mx2, s);
;             }
;             if ((lane & 7) == 0) atomicMax(ctl + CW_KMAX + ((blk * 32) / S) * 8 + (lane >> 3), __float_as_uint(mx2));
.LBB0_556:
	s_add_i32 s2, s1, s9
	s_mul_hi_i32 s3, s2, 0x1c00
	s_mulk_i32 s2, 0x1c00
	s_add_u32 s2, s54, s2
	global_load_dwordx4 v[110:113], v[6:7], off
	s_addc_u32 s3, s55, s3
	v_lshl_add_u64 v[18:19], s[2:3], 0, v[0:1]
	v_add_co_u32_e64 v18, s[2:3], s7, v18
	s_add_i32 s9, s9, 2
	s_nop 0
	v_addc_co_u32_e64 v19, s[2:3], 0, v19, s[2:3]
	global_load_dwordx4 v[114:117], v[18:19], off offset:1024
	v_lshl_add_u64 v[6:7], v[6:7], 0, s[4:5]
	s_add_i32 s2, s1, s9
	s_mul_hi_i32 s3, s2, 0x1c00
	s_mulk_i32 s2, 0x1c00
	s_add_u32 s2, s54, s2
	global_load_dwordx4 v[118:121], v[6:7], off
	s_addc_u32 s3, s55, s3
	v_lshl_add_u64 v[18:19], s[2:3], 0, v[0:1]
	v_add_co_u32_e64 v18, s[2:3], s7, v18
	s_add_i32 s9, s9, 2
	s_nop 0
	v_addc_co_u32_e64 v19, s[2:3], 0, v19, s[2:3]
	global_load_dwordx4 v[122:125], v[18:19], off offset:1024
	v_lshl_add_u64 v[6:7], v[6:7], 0, s[4:5]
	s_add_i32 s2, s1, s9
	s_mul_hi_i32 s3, s2, 0x1c00
	s_mulk_i32 s2, 0x1c00
	s_add_u32 s2, s54, s2
	global_load_dwordx4 v[126:129], v[6:7], off
	s_addc_u32 s3, s55, s3
	v_lshl_add_u64 v[18:19], s[2:3], 0, v[0:1]
	v_add_co_u32_e64 v18, s[2:3], s7, v18
	s_add_i32 s9, s9, 2
	s_nop 0
	v_addc_co_u32_e64 v19, s[2:3], 0, v19, s[2:3]
	global_load_dwordx4 v[130:133], v[18:19], off offset:1024
	v_lshl_add_u64 v[6:7], v[6:7], 0, s[4:5]
	s_add_i32 s2, s1, s9
	s_mul_hi_i32 s3, s2, 0x1c00
	s_mulk_i32 s2, 0x1c00
	s_add_u32 s2, s54, s2
	global_load_dwordx4 v[134:137], v[6:7], off
	s_addc_u32 s3, s55, s3
	v_lshl_add_u64 v[18:19], s[2:3], 0, v[0:1]
	v_add_co_u32_e64 v18, s[2:3], s7, v18
	s_add_i32 s9, s9, 2
	s_nop 0
	v_addc_co_u32_e64 v19, s[2:3], 0, v19, s[2:3]
	global_load_dwordx4 v[138:141], v[18:19], off offset:1024
	v_lshl_add_u64 v[6:7], v[6:7], 0, s[4:5]
	s_add_i32 s2, s1, s9
	s_mul_hi_i32 s3, s2, 0x1c00
	s_mulk_i32 s2, 0x1c00
	s_add_u32 s2, s54, s2
	global_load_dwordx4 v[142:145], v[6:7], off
	s_addc_u32 s3, s55, s3
	v_lshl_add_u64 v[18:19], s[2:3], 0, v[0:1]
	v_add_co_u32_e64 v18, s[2:3], s7, v18
	s_add_i32 s9, s9, 2
	s_nop 0
	v_addc_co_u32_e64 v19, s[2:3], 0, v19, s[2:3]
	global_load_dwordx4 v[146:149], v[18:19], off offset:1024
	v_lshl_add_u64 v[6:7], v[6:7], 0, s[4:5]
	s_add_i32 s2, s1, s9
	s_mul_hi_i32 s3, s2, 0x1c00
	s_mulk_i32 s2, 0x1c00
	s_add_u32 s2, s54, s2
	global_load_dwordx4 v[150:153], v[6:7], off
	s_addc_u32 s3, s55, s3
	v_lshl_add_u64 v[18:19], s[2:3], 0, v[0:1]
	v_add_co_u32_e64 v18, s[2:3], s7, v18
	s_add_i32 s9, s9, 2
	s_nop 0
	v_addc_co_u32_e64 v19, s[2:3], 0, v19, s[2:3]
	global_load_dwordx4 v[154:157], v[18:19], off offset:1024
	v_lshl_add_u64 v[6:7], v[6:7], 0, s[4:5]
	s_add_i32 s2, s1, s9
	s_mul_hi_i32 s3, s2, 0x1c00
	s_mulk_i32 s2, 0x1c00
	s_add_u32 s2, s54, s2
	global_load_dwordx4 v[158:161], v[6:7], off
	s_addc_u32 s3, s55, s3
	v_lshl_add_u64 v[18:19], s[2:3], 0, v[0:1]
	v_add_co_u32_e64 v18, s[2:3], s7, v18
	s_add_i32 s9, s9, 2
	s_nop 0
	v_addc_co_u32_e64 v19, s[2:3], 0, v19, s[2:3]
	global_load_dwordx4 v[162:165], v[18:19], off offset:1024
	v_lshl_add_u64 v[6:7], v[6:7], 0, s[4:5]
	s_add_i32 s2, s1, s9
	s_mul_hi_i32 s3, s2, 0x1c00
	s_mulk_i32 s2, 0x1c00
	s_add_u32 s2, s54, s2
	global_load_dwordx4 v[166:169], v[6:7], off
	s_addc_u32 s3, s55, s3
	v_lshl_add_u64 v[18:19], s[2:3], 0, v[0:1]
	v_add_co_u32_e64 v18, s[2:3], s7, v18
	s_add_i32 s9, s9, 2
	s_nop 0
	v_addc_co_u32_e64 v19, s[2:3], 0, v19, s[2:3]
	global_load_dwordx4 v[170:173], v[18:19], off offset:1024
	v_lshl_add_u64 v[6:7], v[6:7], 0, s[4:5]
	s_waitcnt vmcnt(14)
	v_mov_b32_e32 v14, v110
	v_mov_b32_e32 v15, v111
	v_mov_b32_e32 v16, v112
	v_mov_b32_e32 v17, v113
	v_mov_b32_e32 v18, v114
	v_mov_b32_e32 v19, v115
	v_mov_b32_e32 v20, v116
	v_mov_b32_e32 v21, v117
	v_lshlrev_b32_e32 v13, 16, v14
	v_and_b32_e32 v14, 0xffff0000, v14
	v_fma_f32 v13, v13, v13, 0
	v_lshlrev_b32_e32 v22, 16, v15
	v_fmac_f32_e32 v13, v14, v14
	v_and_b32_e32 v15, 0xffff0000, v15
	v_fmac_f32_e32 v13, v22, v22
	v_lshlrev_b32_e32 v23, 16, v16
	v_fmac_f32_e32 v13, v15, v15
	v_lshlrev_b32_e32 v14, 16, v18
	v_and_b32_e32 v16, 0xffff0000, v16
	v_fmac_f32_e32 v13, v23, v23
	v_and_b32_e32 v15, 0xffff0000, v18
	v_fma_f32 v14, v14, v14, 0
	v_fmac_f32_e32 v13, v16, v16
	v_lshlrev_b32_e32 v16, 16, v19
	v_fmac_f32_e32 v14, v15, v15
	v_and_b32_e32 v18, 0xffff0000, v19
	v_fmac_f32_e32 v14, v16, v16
	v_lshlrev_b32_e32 v19, 16, v20
	v_fmac_f32_e32 v14, v18, v18
	v_and_b32_e32 v20, 0xffff0000, v20
	v_fmac_f32_e32 v14, v19, v19
	v_lshlrev_b32_e32 v24, 16, v17
	v_lshlrev_b32_e32 v22, 16, v21
	v_fmac_f32_e32 v14, v20, v20
	v_and_b32_e32 v17, 0xffff0000, v17
	v_and_b32_e32 v21, 0xffff0000, v21
	v_fmac_f32_e32 v13, v24, v24
	v_fmac_f32_e32 v14, v22, v22
	v_fmac_f32_e32 v13, v17, v17
	v_fmac_f32_e32 v14, v21, v21
	ds_bpermute_b32 v15, v8, v13
	ds_bpermute_b32 v16, v8, v14
	s_waitcnt lgkmcnt(1)
	v_add_f32_e32 v13, v13, v15
	s_waitcnt lgkmcnt(0)
	v_add_f32_e32 v14, v14, v16
	ds_bpermute_b32 v15, v9, v13
	ds_bpermute_b32 v16, v9, v14
	s_waitcnt lgkmcnt(1)
	v_add_f32_e32 v13, v13, v15
	s_waitcnt lgkmcnt(0)
	v_add_f32_e32 v14, v14, v16
	ds_bpermute_b32 v15, v10, v13
	ds_bpermute_b32 v16, v10, v14
	s_waitcnt lgkmcnt(1)
	v_add_f32_e32 v13, v13, v15
	s_waitcnt lgkmcnt(0)
	v_add_f32_e32 v14, v14, v16
	v_max3_f32 v12, v12, v13, v14
	s_add_i32 s2, s1, s9
	s_mul_hi_i32 s3, s2, 0x1c00
	s_mulk_i32 s2, 0x1c00
	s_add_u32 s2, s54, s2
	global_load_dwordx4 v[110:113], v[6:7], off
	s_addc_u32 s3, s55, s3
	v_lshl_add_u64 v[18:19], s[2:3], 0, v[0:1]
	v_add_co_u32_e64 v18, s[2:3], s7, v18
	s_add_i32 s9, s9, 2
	s_nop 0
	v_addc_co_u32_e64 v19, s[2:3], 0, v19, s[2:3]
	global_load_dwordx4 v[114:117], v[18:19], off offset:1024
	v_lshl_add_u64 v[6:7], v[6:7], 0, s[4:5]
	s_waitcnt vmcnt(14)
; template <int PH>
; __device__ __forceinline__ void mk_body(const Args& a) {
;     ...
;                 const u32x4 v = *(const u32x4*)(y0 + (size_t)(blk * 32 + i) * Y0P + Y0_FK + 8 * lane);
;                 float s = 0.f;
; #pragma unroll
;                 for (int j = 0; j < 4; ++j) { const float lo_ = __uint_as_float(v[j] << 16), hi_ = __uint_as_float(v[j] & 0xffff0000u); s = fmaf(lo_, lo_, s); s = fmaf(hi_, hi_, s); }
;                 s += __shfl_xor(s, 1); s += __shfl_xor(s, 2); s += __shfl_xor(s, 4);
;                 mx2 = fmaxf(mx2, s);
	v_mov_b32_e32 v14, v118
	v_mov_b32_e32 v15, v119
	v_mov_b32_e32 v16, v120
	v_mov_b32_e32 v17, v121
	v_mov_b32_e32 v18, v122
	v_mov_b32_e32 v19, v123
	v_mov_b32_e32 v20, v124
	v_mov_b32_e32 v21, v125
	v_lshlrev_b32_e32 v13, 16, v14
	v_and_b32_e32 v14, 0xffff0000, v14
	v_fma_f32 v13, v13, v13, 0
	v_lshlrev_b32_e32 v22, 16, v15
	v_fmac_f32_e32 v13, v14, v14
	v_and_b32_e32 v15, 0xffff0000, v15
	v_fmac_f32_e32 v13, v22, v22
	v_lshlrev_b32_e32 v23, 16, v16
	v_fmac_f32_e32 v13, v15, v15
	v_lshlrev_b32_e32 v14, 16, v18
	v_and_b32_e32 v16, 0xffff0000, v16
	v_fmac_f32_e32 v13, v23, v23
	v_and_b32_e32 v15, 0xffff0000, v18
	v_fma_f32 v14, v14, v14, 0
	v_fmac_f32_e32 v13, v16, v16
	v_lshlrev_b32_e32 v16, 16, v19
	v_fmac_f32_e32 v14, v15, v15
	v_and_b32_e32 v18, 0xffff0000, v19
	v_fmac_f32_e32 v14, v16, v16
	v_lshlrev_b32_e32 v19, 16, v20
	v_fmac_f32_e32 v14, v18, v18
	v_and_b32_e32 v20, 0xffff0000, v20
	v_fmac_f32_e32 v14, v19, v19
	v_lshlrev_b32_e32 v24, 16, v17
	v_lshlrev_b32_e32 v22, 16, v21
	v_fmac_f32_e32 v14, v20, v20
	v_and_b32_e32 v17, 0xffff0000, v17
	v_and_b32_e32 v21, 0xffff0000, v21
	v_fmac_f32_e32 v13, v24, v24
	v_fmac_f32_e32 v14, v22, v22
	v_fmac_f32_e32 v13, v17, v17
	v_fmac_f32_e32 v14, v21, v21
	ds_bpermute_b32 v15, v8, v13
	ds_bpermute_b32 v16, v8, v14
	s_waitcnt lgkmcnt(1)
	v_add_f32_e32 v13, v13, v15
	s_waitcnt lgkmcnt(0)
	v_add_f32_e32 v14, v14, v16
	ds_bpermute_b32 v15, v9, v13
	ds_bpermute_b32 v16, v9, v14
	s_waitcnt lgkmcnt(1)
	v_add_f32_e32 v13, v13, v15
	s_waitcnt lgkmcnt(0)
	v_add_f32_e32 v14, v14, v16
	ds_bpermute_b32 v15, v10, v13
	ds_bpermute_b32 v16, v10, v14
	s_waitcnt lgkmcnt(1)
	v_add_f32_e32 v13, v13, v15
	s_waitcnt lgkmcnt(0)
	v_add_f32_e32 v14, v14, v16
	v_max3_f32 v12, v12, v13, v14
	s_add_i32 s2, s1, s9
	s_mul_hi_i32 s3, s2, 0x1c00
	s_mulk_i32 s2, 0x1c00
	s_add_u32 s2, s54, s2
	global_load_dwordx4 v[118:121], v[6:7], off
	s_addc_u32 s3, s55, s3
	v_lshl_add_u64 v[18:19], s[2:3], 0, v[0:1]
	v_add_co_u32_e64 v18, s[2:3], s7, v18
	s_add_i32 s9, s9, 2
	s_nop 0
	v_addc_co_u32_e64 v19, s[2:3], 0, v19, s[2:3]
	global_load_dwordx4 v[122:125], v[18:19], off offset:1024
	v_lshl_add_u64 v[6:7], v[6:7], 0, s[4:5]
	s_waitcnt vmcnt(14)
	v_mov_b32_e32 v14, v126
	v_mov_b32_e32 v15, v127
	v_mov_b32_e32 v16, v128
	v_mov_b32_e32 v17, v129
	v_mov_b32_e32 v18, v130
	v_mov_b32_e32 v19, v131
	v_mov_b32_e32 v20, v132
	v_mov_b32_e32 v21, v133
	v_lshlrev_b32_e32 v13, 16, v14
	v_and_b32_e32 v14, 0xffff0000, v14
	v_fma_f32 v13, v13, v13, 0
	v_lshlrev_b32_e32 v22, 16, v15
	v_fmac_f32_e32 v13, v14, v14
	v_and_b32_e32 v15, 0xffff0000, v15
	v_fmac_f32_e32 v13, v22, v22
	v_lshlrev_b32_e32 v23, 16, v16
	v_fmac_f32_e32 v13, v15, v15
	v_lshlrev_b32_e32 v14, 16, v18
	v_and_b32_e32 v16, 0xffff0000, v16
	v_fmac_f32_e32 v13, v23, v23
	v_and_b32_e32 v15, 0xffff0000, v18
	v_fma_f32 v14, v14, v14, 0
	v_fmac_f32_e32 v13, v16, v16
	v_lshlrev_b32_e32 v16, 16, v19
	v_fmac_f32_e32 v14, v15, v15
	v_and_b32_e32 v18, 0xffff0000, v19
	v_fmac_f32_e32 v14, v16, v16
	v_lshlrev_b32_e32 v19, 16, v20
	v_fmac_f32_e32 v14, v18, v18
	v_and_b32_e32 v20, 0xffff0000, v20
	v_fmac_f32_e32 v14, v19, v19
	v_lshlrev_b32_e32 v24, 16, v17
	v_lshlrev_b32_e32 v22, 16, v21
	v_fmac_f32_e32 v14, v20, v20
	v_and_b32_e32 v17, 0xffff0000, v17
	v_and_b32_e32 v21, 0xffff0000, v21
	v_fmac_f32_e32 v13, v24, v24
	v_fmac_f32_e32 v14, v22, v22
	v_fmac_f32_e32 v13, v17, v17
	v_fmac_f32_e32 v14, v21, v21
	ds_bpermute_b32 v15, v8, v13
	ds_bpermute_b32 v16, v8, v14
	s_waitcnt lgkmcnt(1)
	v_add_f32_e32 v13, v13, v15
	s_waitcnt lgkmcnt(0)
	v_add_f32_e32 v14, v14, v16
	ds_bpermute_b32 v15, v9, v13
	ds_bpermute_b32 v16, v9, v14
	s_waitcnt lgkmcnt(1)
	v_add_f32_e32 v13, v13, v15
	s_waitcnt lgkmcnt(0)
	v_add_f32_e32 v14, v14, v16
	ds_bpermute_b32 v15, v10, v13
	ds_bpermute_b32 v16, v10, v14
	s_waitcnt lgkmcnt(1)
	v_add_f32_e32 v13, v13, v15
	s_waitcnt lgkmcnt(0)
	v_add_f32_e32 v14, v14, v16
	v_max3_f32 v12, v12, v13, v14
	s_add_i32 s2, s1, s9
	s_mul_hi_i32 s3, s2, 0x1c00
	s_mulk_i32 s2, 0x1c00
	s_add_u32 s2, s54, s2
	global_load_dwordx4 v[126:129], v[6:7], off
	s_addc_u32 s3, s55, s3
	v_lshl_add_u64 v[18:19], s[2:3], 0, v[0:1]
	v_add_co_u32_e64 v18, s[2:3], s7, v18
	s_add_i32 s9, s9, 2
	s_nop 0
	v_addc_co_u32_e64 v19, s[2:3], 0, v19, s[2:3]
	global_load_dwordx4 v[130:133], v[18:19], off offset:1024
	v_lshl_add_u64 v[6:7], v[6:7], 0, s[4:5]
	s_waitcnt vmcnt(14)
	v_mov_b32_e32 v14, v134
	v_mov_b32_e32 v15, v135
	v_mov_b32_e32 v16, v136
	v_mov_b32_e32 v17, v137
	v_mov_b32_e32 v18, v138
	v_mov_b32_e32 v19, v139
	v_mov_b32_e32 v20, v140
	v_mov_b32_e32 v21, v141
	v_lshlrev_b32_e32 v13, 16, v14
	v_and_b32_e32 v14, 0xffff0000, v14
	v_fma_f32 v13, v13, v13, 0
	v_lshlrev_b32_e32 v22, 16, v15
	v_fmac_f32_e32 v13, v14, v14
	v_and_b32_e32 v15, 0xffff0000, v15
	v_fmac_f32_e32 v13, v22, v22
	v_lshlrev_b32_e32 v23, 16, v16
	v_fmac_f32_e32 v13, v15, v15
	v_lshlrev_b32_e32 v14, 16, v18
	v_and_b32_e32 v16, 0xffff0000, v16
	v_fmac_f32_e32 v13, v23, v23
	v_and_b32_e32 v15, 0xffff0000, v18
	v_fma_f32 v14, v14, v14, 0
	v_fmac_f32_e32 v13, v16, v16
	v_lshlrev_b32_e32 v16, 16, v19
	v_fmac_f32_e32 v14, v15, v15
	v_and_b32_e32 v18, 0xffff0000, v19
	v_fmac_f32_e32 v14, v16, v16
	v_lshlrev_b32_e32 v19, 16, v20
	v_fmac_f32_e32 v14, v18, v18
	v_and_b32_e32 v20, 0xffff0000, v20
	v_fmac_f32_e32 v14, v19, v19
	v_lshlrev_b32_e32 v24, 16, v17
	v_lshlrev_b32_e32 v22, 16, v21
	v_fmac_f32_e32 v14, v20, v20
	v_and_b32_e32 v17, 0xffff0000, v17
	v_and_b32_e32 v21, 0xffff0000, v21
	v_fmac_f32_e32 v13, v24, v24
	v_fmac_f32_e32 v14, v22, v22
	v_fmac_f32_e32 v13, v17, v17
	v_fmac_f32_e32 v14, v21, v21
	ds_bpermute_b32 v15, v8, v13
	ds_bpermute_b32 v16, v8, v14
	s_waitcnt lgkmcnt(1)
; template <int PH>
; __device__ __forceinline__ void mk_body(const Args& a) {
;     ...
;                 const u32x4 v = *(const u32x4*)(y0 + (size_t)(blk * 32 + i) * Y0P + Y0_FK + 8 * lane);
;                 float s = 0.f;
; #pragma unroll
;                 for (int j = 0; j < 4; ++j) { const float lo_ = __uint_as_float(v[j] << 16), hi_ = __uint_as_float(v[j] & 0xffff0000u); s = fmaf(lo_, lo_, s); s = fmaf(hi_, hi_, s); }
;                 s += __shfl_xor(s, 1); s += __shfl_xor(s, 2); s += __shfl_xor(s, 4);
;                 mx2 = fmaxf(mx2, s);
	v_add_f32_e32 v13, v13, v15
	s_waitcnt lgkmcnt(0)
	v_add_f32_e32 v14, v14, v16
	ds_bpermute_b32 v15, v9, v13
	ds_bpermute_b32 v16, v9, v14
	s_waitcnt lgkmcnt(1)
	v_add_f32_e32 v13, v13, v15
	s_waitcnt lgkmcnt(0)
	v_add_f32_e32 v14, v14, v16
	ds_bpermute_b32 v15, v10, v13
	ds_bpermute_b32 v16, v10, v14
	s_waitcnt lgkmcnt(1)
	v_add_f32_e32 v13, v13, v15
	s_waitcnt lgkmcnt(0)
	v_add_f32_e32 v14, v14, v16
	v_max3_f32 v12, v12, v13, v14
	s_add_i32 s2, s1, s9
	s_mul_hi_i32 s3, s2, 0x1c00
	s_mulk_i32 s2, 0x1c00
	s_add_u32 s2, s54, s2
	global_load_dwordx4 v[134:137], v[6:7], off
	s_addc_u32 s3, s55, s3
	v_lshl_add_u64 v[18:19], s[2:3], 0, v[0:1]
	v_add_co_u32_e64 v18, s[2:3], s7, v18
	s_add_i32 s9, s9, 2
	s_nop 0
	v_addc_co_u32_e64 v19, s[2:3], 0, v19, s[2:3]
	global_load_dwordx4 v[138:141], v[18:19], off offset:1024
	v_lshl_add_u64 v[6:7], v[6:7], 0, s[4:5]
	s_waitcnt vmcnt(14)
	v_mov_b32_e32 v14, v142
	v_mov_b32_e32 v15, v143
	v_mov_b32_e32 v16, v144
	v_mov_b32_e32 v17, v145
	v_mov_b32_e32 v18, v146
	v_mov_b32_e32 v19, v147
	v_mov_b32_e32 v20, v148
	v_mov_b32_e32 v21, v149
	v_lshlrev_b32_e32 v13, 16, v14
	v_and_b32_e32 v14, 0xffff0000, v14
	v_fma_f32 v13, v13, v13, 0
	v_lshlrev_b32_e32 v22, 16, v15
	v_fmac_f32_e32 v13, v14, v14
	v_and_b32_e32 v15, 0xffff0000, v15
	v_fmac_f32_e32 v13, v22, v22
	v_lshlrev_b32_e32 v23, 16, v16
	v_fmac_f32_e32 v13, v15, v15
	v_lshlrev_b32_e32 v14, 16, v18
	v_and_b32_e32 v16, 0xffff0000, v16
	v_fmac_f32_e32 v13, v23, v23
	v_and_b32_e32 v15, 0xffff0000, v18
	v_fma_f32 v14, v14, v14, 0
	v_fmac_f32_e32 v13, v16, v16
	v_lshlrev_b32_e32 v16, 16, v19
	v_fmac_f32_e32 v14, v15, v15
	v_and_b32_e32 v18, 0xffff0000, v19
	v_fmac_f32_e32 v14, v16, v16
	v_lshlrev_b32_e32 v19, 16, v20
	v_fmac_f32_e32 v14, v18, v18
	v_and_b32_e32 v20, 0xffff0000, v20
	v_fmac_f32_e32 v14, v19, v19
	v_lshlrev_b32_e32 v24, 16, v17
	v_lshlrev_b32_e32 v22, 16, v21
	v_fmac_f32_e32 v14, v20, v20
	v_and_b32_e32 v17, 0xffff0000, v17
	v_and_b32_e32 v21, 0xffff0000, v21
	v_fmac_f32_e32 v13, v24, v24
	v_fmac_f32_e32 v14, v22, v22
	v_fmac_f32_e32 v13, v17, v17
	v_fmac_f32_e32 v14, v21, v21
	ds_bpermute_b32 v15, v8, v13
	ds_bpermute_b32 v16, v8, v14
	s_waitcnt lgkmcnt(1)
	v_add_f32_e32 v13, v13, v15
	s_waitcnt lgkmcnt(0)
	v_add_f32_e32 v14, v14, v16
	ds_bpermute_b32 v15, v9, v13
	ds_bpermute_b32 v16, v9, v14
	s_waitcnt lgkmcnt(1)
	v_add_f32_e32 v13, v13, v15
	s_waitcnt lgkmcnt(0)
	v_add_f32_e32 v14, v14, v16
	ds_bpermute_b32 v15, v10, v13
	ds_bpermute_b32 v16, v10, v14
	s_waitcnt lgkmcnt(1)
	v_add_f32_e32 v13, v13, v15
	s_waitcnt lgkmcnt(0)
	v_add_f32_e32 v14, v14, v16
	v_max3_f32 v12, v12, v13, v14
	s_add_i32 s2, s1, s9
	s_mul_hi_i32 s3, s2, 0x1c00
	s_mulk_i32 s2, 0x1c00
	s_add_u32 s2, s54, s2
	global_load_dwordx4 v[142:145], v[6:7], off
	s_addc_u32 s3, s55, s3
	v_lshl_add_u64 v[18:19], s[2:3], 0, v[0:1]
	v_add_co_u32_e64 v18, s[2:3], s7, v18
	s_add_i32 s9, s9, 2
	s_nop 0
	v_addc_co_u32_e64 v19, s[2:3], 0, v19, s[2:3]
	global_load_dwordx4 v[146:149], v[18:19], off offset:1024
	v_lshl_add_u64 v[6:7], v[6:7], 0, s[4:5]
	s_waitcnt vmcnt(14)
	v_mov_b32_e32 v14, v150
	v_mov_b32_e32 v15, v151
	v_mov_b32_e32 v16, v152
	v_mov_b32_e32 v17, v153
	v_mov_b32_e32 v18, v154
	v_mov_b32_e32 v19, v155
	v_mov_b32_e32 v20, v156
	v_mov_b32_e32 v21, v157
	v_lshlrev_b32_e32 v13, 16, v14
	v_and_b32_e32 v14, 0xffff0000, v14
	v_fma_f32 v13, v13, v13, 0
	v_lshlrev_b32_e32 v22, 16, v15
	v_fmac_f32_e32 v13, v14, v14
	v_and_b32_e32 v15, 0xffff0000, v15
	v_fmac_f32_e32 v13, v22, v22
	v_lshlrev_b32_e32 v23, 16, v16
	v_fmac_f32_e32 v13, v15, v15
	v_lshlrev_b32_e32 v14, 16, v18
	v_and_b32_e32 v16, 0xffff0000, v16
	v_fmac_f32_e32 v13, v23, v23
	v_and_b32_e32 v15, 0xffff0000, v18
	v_fma_f32 v14, v14, v14, 0
	v_fmac_f32_e32 v13, v16, v16
	v_lshlrev_b32_e32 v16, 16, v19
	v_fmac_f32_e32 v14, v15, v15
	v_and_b32_e32 v18, 0xffff0000, v19
	v_fmac_f32_e32 v14, v16, v16
	v_lshlrev_b32_e32 v19, 16, v20
	v_fmac_f32_e32 v14, v18, v18
	v_and_b32_e32 v20, 0xffff0000, v20
	v_fmac_f32_e32 v14, v19, v19
	v_lshlrev_b32_e32 v24, 16, v17
	v_lshlrev_b32_e32 v22, 16, v21
	v_fmac_f32_e32 v14, v20, v20
	v_and_b32_e32 v17, 0xffff0000, v17
	v_and_b32_e32 v21, 0xffff0000, v21
	v_fmac_f32_e32 v13, v24, v24
	v_fmac_f32_e32 v14, v22, v22
	v_fmac_f32_e32 v13, v17, v17
	v_fmac_f32_e32 v14, v21, v21
	ds_bpermute_b32 v15, v8, v13
	ds_bpermute_b32 v16, v8, v14
	s_waitcnt lgkmcnt(1)
	v_add_f32_e32 v13, v13, v15
	s_waitcnt lgkmcnt(0)
	v_add_f32_e32 v14, v14, v16
	ds_bpermute_b32 v15, v9, v13
	ds_bpermute_b32 v16, v9, v14
	s_waitcnt lgkmcnt(1)
	v_add_f32_e32 v13, v13, v15
	s_waitcnt lgkmcnt(0)
	v_add_f32_e32 v14, v14, v16
	ds_bpermute_b32 v15, v10, v13
	ds_bpermute_b32 v16, v10, v14
	s_waitcnt lgkmcnt(1)
	v_add_f32_e32 v13, v13, v15
	s_waitcnt lgkmcnt(0)
	v_add_f32_e32 v14, v14, v16
	v_max3_f32 v12, v12, v13, v14
	s_add_i32 s2, s1, s9
	s_mul_hi_i32 s3, s2, 0x1c00
	s_mulk_i32 s2, 0x1c00
	s_add_u32 s2, s54, s2
	global_load_dwordx4 v[150:153], v[6:7], off
	s_addc_u32 s3, s55, s3
	v_lshl_add_u64 v[18:19], s[2:3], 0, v[0:1]
	v_add_co_u32_e64 v18, s[2:3], s7, v18
	s_add_i32 s9, s9, 2
	s_nop 0
	v_addc_co_u32_e64 v19, s[2:3], 0, v19, s[2:3]
	global_load_dwordx4 v[154:157], v[18:19], off offset:1024
	v_lshl_add_u64 v[6:7], v[6:7], 0, s[4:5]
	s_waitcnt vmcnt(14)
; template <int PH>
; __device__ __forceinline__ void mk_body(const Args& a) {
;     ...
;                 const u32x4 v = *(const u32x4*)(y0 + (size_t)(blk * 32 + i) * Y0P + Y0_FK + 8 * lane);
;                 float s = 0.f;
; #pragma unroll
;                 for (int j = 0; j < 4; ++j) { const float lo_ = __uint_as_float(v[j] << 16), hi_ = __uint_as_float(v[j] & 0xffff0000u); s = fmaf(lo_, lo_, s); s = fmaf(hi_, hi_, s); }
;                 s += __shfl_xor(s, 1); s += __shfl_xor(s, 2); s += __shfl_xor(s, 4);
;                 mx2 = fmaxf(mx2, s);
	v_mov_b32_e32 v14, v158
	v_mov_b32_e32 v15, v159
	v_mov_b32_e32 v16, v160
	v_mov_b32_e32 v17, v161
	v_mov_b32_e32 v18, v162
	v_mov_b32_e32 v19, v163
	v_mov_b32_e32 v20, v164
	v_mov_b32_e32 v21, v165
	v_lshlrev_b32_e32 v13, 16, v14
	v_and_b32_e32 v14, 0xffff0000, v14
	v_fma_f32 v13, v13, v13, 0
	v_lshlrev_b32_e32 v22, 16, v15
	v_fmac_f32_e32 v13, v14, v14
	v_and_b32_e32 v15, 0xffff0000, v15
	v_fmac_f32_e32 v13, v22, v22
	v_lshlrev_b32_e32 v23, 16, v16
	v_fmac_f32_e32 v13, v15, v15
	v_lshlrev_b32_e32 v14, 16, v18
	v_and_b32_e32 v16, 0xffff0000, v16
	v_fmac_f32_e32 v13, v23, v23
	v_and_b32_e32 v15, 0xffff0000, v18
	v_fma_f32 v14, v14, v14, 0
	v_fmac_f32_e32 v13, v16, v16
	v_lshlrev_b32_e32 v16, 16, v19
	v_fmac_f32_e32 v14, v15, v15
	v_and_b32_e32 v18, 0xffff0000, v19
	v_fmac_f32_e32 v14, v16, v16
	v_lshlrev_b32_e32 v19, 16, v20
	v_fmac_f32_e32 v14, v18, v18
	v_and_b32_e32 v20, 0xffff0000, v20
	v_fmac_f32_e32 v14, v19, v19
	v_lshlrev_b32_e32 v24, 16, v17
	v_lshlrev_b32_e32 v22, 16, v21
	v_fmac_f32_e32 v14, v20, v20
	v_and_b32_e32 v17, 0xffff0000, v17
	v_and_b32_e32 v21, 0xffff0000, v21
	v_fmac_f32_e32 v13, v24, v24
	v_fmac_f32_e32 v14, v22, v22
	v_fmac_f32_e32 v13, v17, v17
	v_fmac_f32_e32 v14, v21, v21
	ds_bpermute_b32 v15, v8, v13
	ds_bpermute_b32 v16, v8, v14
	s_waitcnt lgkmcnt(1)
	v_add_f32_e32 v13, v13, v15
	s_waitcnt lgkmcnt(0)
	v_add_f32_e32 v14, v14, v16
	ds_bpermute_b32 v15, v9, v13
	ds_bpermute_b32 v16, v9, v14
	s_waitcnt lgkmcnt(1)
	v_add_f32_e32 v13, v13, v15
	s_waitcnt lgkmcnt(0)
	v_add_f32_e32 v14, v14, v16
	ds_bpermute_b32 v15, v10, v13
	ds_bpermute_b32 v16, v10, v14
	s_waitcnt lgkmcnt(1)
	v_add_f32_e32 v13, v13, v15
	s_waitcnt lgkmcnt(0)
	v_add_f32_e32 v14, v14, v16
	v_max3_f32 v12, v12, v13, v14
	s_add_i32 s2, s1, s9
	s_mul_hi_i32 s3, s2, 0x1c00
	s_mulk_i32 s2, 0x1c00
	s_add_u32 s2, s54, s2
	global_load_dwordx4 v[158:161], v[6:7], off
	s_addc_u32 s3, s55, s3
	v_lshl_add_u64 v[18:19], s[2:3], 0, v[0:1]
	v_add_co_u32_e64 v18, s[2:3], s7, v18
	s_add_i32 s9, s9, 2
	s_nop 0
	v_addc_co_u32_e64 v19, s[2:3], 0, v19, s[2:3]
	global_load_dwordx4 v[162:165], v[18:19], off offset:1024
	v_lshl_add_u64 v[6:7], v[6:7], 0, s[4:5]
	s_waitcnt vmcnt(14)
	v_mov_b32_e32 v14, v166
	v_mov_b32_e32 v15, v167
	v_mov_b32_e32 v16, v168
	v_mov_b32_e32 v17, v169
	v_mov_b32_e32 v18, v170
	v_mov_b32_e32 v19, v171
	v_mov_b32_e32 v20, v172
	v_mov_b32_e32 v21, v173
	v_lshlrev_b32_e32 v13, 16, v14
	v_and_b32_e32 v14, 0xffff0000, v14
	v_fma_f32 v13, v13, v13, 0
	v_lshlrev_b32_e32 v22, 16, v15
	v_fmac_f32_e32 v13, v14, v14
	v_and_b32_e32 v15, 0xffff0000, v15
	v_fmac_f32_e32 v13, v22, v22
	v_lshlrev_b32_e32 v23, 16, v16
	v_fmac_f32_e32 v13, v15, v15
	v_lshlrev_b32_e32 v14, 16, v18
	v_and_b32_e32 v16, 0xffff0000, v16
	v_fmac_f32_e32 v13, v23, v23
	v_and_b32_e32 v15, 0xffff0000, v18
	v_fma_f32 v14, v14, v14, 0
	v_fmac_f32_e32 v13, v16, v16
	v_lshlrev_b32_e32 v16, 16, v19
	v_fmac_f32_e32 v14, v15, v15
	v_and_b32_e32 v18, 0xffff0000, v19
	v_fmac_f32_e32 v14, v16, v16
	v_lshlrev_b32_e32 v19, 16, v20
	v_fmac_f32_e32 v14, v18, v18
	v_and_b32_e32 v20, 0xffff0000, v20
	v_fmac_f32_e32 v14, v19, v19
	v_lshlrev_b32_e32 v24, 16, v17
	v_lshlrev_b32_e32 v22, 16, v21
	v_fmac_f32_e32 v14, v20, v20
	v_and_b32_e32 v17, 0xffff0000, v17
	v_and_b32_e32 v21, 0xffff0000, v21
	v_fmac_f32_e32 v13, v24, v24
	v_fmac_f32_e32 v14, v22, v22
	v_fmac_f32_e32 v13, v17, v17
	v_fmac_f32_e32 v14, v21, v21
	ds_bpermute_b32 v15, v8, v13
	ds_bpermute_b32 v16, v8, v14
	s_waitcnt lgkmcnt(1)
	v_add_f32_e32 v13, v13, v15
	s_waitcnt lgkmcnt(0)
	v_add_f32_e32 v14, v14, v16
	ds_bpermute_b32 v15, v9, v13
	ds_bpermute_b32 v16, v9, v14
	s_waitcnt lgkmcnt(1)
	v_add_f32_e32 v13, v13, v15
	s_waitcnt lgkmcnt(0)
	v_add_f32_e32 v14, v14, v16
	ds_bpermute_b32 v15, v10, v13
	ds_bpermute_b32 v16, v10, v14
	s_waitcnt lgkmcnt(1)
	v_add_f32_e32 v13, v13, v15
	s_waitcnt lgkmcnt(0)
	v_add_f32_e32 v14, v14, v16
	v_max3_f32 v12, v12, v13, v14
	s_add_i32 s2, s1, s9
	s_mul_hi_i32 s3, s2, 0x1c00
	s_mulk_i32 s2, 0x1c00
	s_add_u32 s2, s54, s2
	global_load_dwordx4 v[166:169], v[6:7], off
	s_addc_u32 s3, s55, s3
	v_lshl_add_u64 v[18:19], s[2:3], 0, v[0:1]
	v_add_co_u32_e64 v18, s[2:3], s7, v18
	s_add_i32 s9, s9, 2
	s_nop 0
	v_addc_co_u32_e64 v19, s[2:3], 0, v19, s[2:3]
	global_load_dwordx4 v[170:173], v[18:19], off offset:1024
	v_lshl_add_u64 v[6:7], v[6:7], 0, s[4:5]
	s_waitcnt vmcnt(14)
	v_mov_b32_e32 v14, v110
	v_mov_b32_e32 v15, v111
	v_mov_b32_e32 v16, v112
	v_mov_b32_e32 v17, v113
	v_mov_b32_e32 v18, v114
	v_mov_b32_e32 v19, v115
	v_mov_b32_e32 v20, v116
	v_mov_b32_e32 v21, v117
	v_lshlrev_b32_e32 v13, 16, v14
	v_and_b32_e32 v14, 0xffff0000, v14
	v_fma_f32 v13, v13, v13, 0
	v_lshlrev_b32_e32 v22, 16, v15
	v_fmac_f32_e32 v13, v14, v14
	v_and_b32_e32 v15, 0xffff0000, v15
	v_fmac_f32_e32 v13, v22, v22
	v_lshlrev_b32_e32 v23, 16, v16
	v_fmac_f32_e32 v13, v15, v15
	v_lshlrev_b32_e32 v14, 16, v18
	v_and_b32_e32 v16, 0xffff0000, v16
	v_fmac_f32_e32 v13, v23, v23
	v_and_b32_e32 v15, 0xffff0000, v18
	v_fma_f32 v14, v14, v14, 0
	v_fmac_f32_e32 v13, v16, v16
	v_lshlrev_b32_e32 v16, 16, v19
	v_fmac_f32_e32 v14, v15, v15
	v_and_b32_e32 v18, 0xffff0000, v19
	v_fmac_f32_e32 v14, v16, v16
	v_lshlrev_b32_e32 v19, 16, v20
	v_fmac_f32_e32 v14, v18, v18
	v_and_b32_e32 v20, 0xffff0000, v20
	v_fmac_f32_e32 v14, v19, v19
	v_lshlrev_b32_e32 v24, 16, v17
	v_lshlrev_b32_e32 v22, 16, v21
	v_fmac_f32_e32 v14, v20, v20
	v_and_b32_e32 v17, 0xffff0000, v17
	v_and_b32_e32 v21, 0xffff0000, v21
	v_fmac_f32_e32 v13, v24, v24
	v_fmac_f32_e32 v14, v22, v22
	v_fmac_f32_e32 v13, v17, v17
	v_fmac_f32_e32 v14, v21, v21
	ds_bpermute_b32 v15, v8, v13
	ds_bpermute_b32 v16, v8, v14
	s_waitcnt lgkmcnt(1)
; template <int PH>
; __device__ __forceinline__ void mk_body(const Args& a) {
;     ...
;                 const u32x4 v = *(const u32x4*)(y0 + (size_t)(blk * 32 + i) * Y0P + Y0_FK + 8 * lane);
;                 float s = 0.f;
; #pragma unroll
;                 for (int j = 0; j < 4; ++j) { const float lo_ = __uint_as_float(v[j] << 16), hi_ = __uint_as_float(v[j] & 0xffff0000u); s = fmaf(lo_, lo_, s); s = fmaf(hi_, hi_, s); }
;                 s += __shfl_xor(s, 1); s += __shfl_xor(s, 2); s += __shfl_xor(s, 4);
;                 mx2 = fmaxf(mx2, s);
	v_add_f32_e32 v13, v13, v15
	s_waitcnt lgkmcnt(0)
	v_add_f32_e32 v14, v14, v16
	ds_bpermute_b32 v15, v9, v13
	ds_bpermute_b32 v16, v9, v14
	s_waitcnt lgkmcnt(1)
	v_add_f32_e32 v13, v13, v15
	s_waitcnt lgkmcnt(0)
	v_add_f32_e32 v14, v14, v16
	ds_bpermute_b32 v15, v10, v13
	ds_bpermute_b32 v16, v10, v14
	s_waitcnt lgkmcnt(1)
	v_add_f32_e32 v13, v13, v15
	s_waitcnt lgkmcnt(0)
	v_add_f32_e32 v14, v14, v16
	v_max3_f32 v12, v12, v13, v14
	s_waitcnt vmcnt(12)
	v_mov_b32_e32 v14, v118
	v_mov_b32_e32 v15, v119
	v_mov_b32_e32 v16, v120
	v_mov_b32_e32 v17, v121
	v_mov_b32_e32 v18, v122
	v_mov_b32_e32 v19, v123
	v_mov_b32_e32 v20, v124
	v_mov_b32_e32 v21, v125
	v_lshlrev_b32_e32 v13, 16, v14
	v_and_b32_e32 v14, 0xffff0000, v14
	v_fma_f32 v13, v13, v13, 0
	v_lshlrev_b32_e32 v22, 16, v15
	v_fmac_f32_e32 v13, v14, v14
	v_and_b32_e32 v15, 0xffff0000, v15
	v_fmac_f32_e32 v13, v22, v22
	v_lshlrev_b32_e32 v23, 16, v16
	v_fmac_f32_e32 v13, v15, v15
	v_lshlrev_b32_e32 v14, 16, v18
	v_and_b32_e32 v16, 0xffff0000, v16
	v_fmac_f32_e32 v13, v23, v23
	v_and_b32_e32 v15, 0xffff0000, v18
	v_fma_f32 v14, v14, v14, 0
	v_fmac_f32_e32 v13, v16, v16
	v_lshlrev_b32_e32 v16, 16, v19
	v_fmac_f32_e32 v14, v15, v15
	v_and_b32_e32 v18, 0xffff0000, v19
	v_fmac_f32_e32 v14, v16, v16
	v_lshlrev_b32_e32 v19, 16, v20
	v_fmac_f32_e32 v14, v18, v18
	v_and_b32_e32 v20, 0xffff0000, v20
	v_fmac_f32_e32 v14, v19, v19
	v_lshlrev_b32_e32 v24, 16, v17
	v_lshlrev_b32_e32 v22, 16, v21
	v_fmac_f32_e32 v14, v20, v20
	v_and_b32_e32 v17, 0xffff0000, v17
	v_and_b32_e32 v21, 0xffff0000, v21
	v_fmac_f32_e32 v13, v24, v24
	v_fmac_f32_e32 v14, v22, v22
	v_fmac_f32_e32 v13, v17, v17
	v_fmac_f32_e32 v14, v21, v21
	ds_bpermute_b32 v15, v8, v13
	ds_bpermute_b32 v16, v8, v14
	s_waitcnt lgkmcnt(1)
	v_add_f32_e32 v13, v13, v15
	s_waitcnt lgkmcnt(0)
	v_add_f32_e32 v14, v14, v16
	ds_bpermute_b32 v15, v9, v13
	ds_bpermute_b32 v16, v9, v14
	s_waitcnt lgkmcnt(1)
	v_add_f32_e32 v13, v13, v15
	s_waitcnt lgkmcnt(0)
	v_add_f32_e32 v14, v14, v16
	ds_bpermute_b32 v15, v10, v13
	ds_bpermute_b32 v16, v10, v14
	s_waitcnt lgkmcnt(1)
	v_add_f32_e32 v13, v13, v15
	s_waitcnt lgkmcnt(0)
	v_add_f32_e32 v14, v14, v16
	v_max3_f32 v12, v12, v13, v14
	s_waitcnt vmcnt(10)
	v_mov_b32_e32 v14, v126
	v_mov_b32_e32 v15, v127
	v_mov_b32_e32 v16, v128
	v_mov_b32_e32 v17, v129
	v_mov_b32_e32 v18, v130
	v_mov_b32_e32 v19, v131
	v_mov_b32_e32 v20, v132
	v_mov_b32_e32 v21, v133
	v_lshlrev_b32_e32 v13, 16, v14
	v_and_b32_e32 v14, 0xffff0000, v14
	v_fma_f32 v13, v13, v13, 0
	v_lshlrev_b32_e32 v22, 16, v15
	v_fmac_f32_e32 v13, v14, v14
	v_and_b32_e32 v15, 0xffff0000, v15
	v_fmac_f32_e32 v13, v22, v22
	v_lshlrev_b32_e32 v23, 16, v16
	v_fmac_f32_e32 v13, v15, v15
	v_lshlrev_b32_e32 v14, 16, v18
	v_and_b32_e32 v16, 0xffff0000, v16
	v_fmac_f32_e32 v13, v23, v23
	v_and_b32_e32 v15, 0xffff0000, v18
	v_fma_f32 v14, v14, v14, 0
	v_fmac_f32_e32 v13, v16, v16
	v_lshlrev_b32_e32 v16, 16, v19
	v_fmac_f32_e32 v14, v15, v15
	v_and_b32_e32 v18, 0xffff0000, v19
	v_fmac_f32_e32 v14, v16, v16
	v_lshlrev_b32_e32 v19, 16, v20
	v_fmac_f32_e32 v14, v18, v18
	v_and_b32_e32 v20, 0xffff0000, v20
	v_fmac_f32_e32 v14, v19, v19
	v_lshlrev_b32_e32 v24, 16, v17
	v_lshlrev_b32_e32 v22, 16, v21
	v_fmac_f32_e32 v14, v20, v20
	v_and_b32_e32 v17, 0xffff0000, v17
	v_and_b32_e32 v21, 0xffff0000, v21
	v_fmac_f32_e32 v13, v24, v24
	v_fmac_f32_e32 v14, v22, v22
	v_fmac_f32_e32 v13, v17, v17
	v_fmac_f32_e32 v14, v21, v21
	ds_bpermute_b32 v15, v8, v13
	ds_bpermute_b32 v16, v8, v14
	s_waitcnt lgkmcnt(1)
	v_add_f32_e32 v13, v13, v15
	s_waitcnt lgkmcnt(0)
	v_add_f32_e32 v14, v14, v16
	ds_bpermute_b32 v15, v9, v13
	ds_bpermute_b32 v16, v9, v14
	s_waitcnt lgkmcnt(1)
	v_add_f32_e32 v13, v13, v15
	s_waitcnt lgkmcnt(0)
	v_add_f32_e32 v14, v14, v16
	ds_bpermute_b32 v15, v10, v13
	ds_bpermute_b32 v16, v10, v14
	s_waitcnt lgkmcnt(1)
	v_add_f32_e32 v13, v13, v15
	s_waitcnt lgkmcnt(0)
	v_add_f32_e32 v14, v14, v16
	v_max3_f32 v12, v12, v13, v14
	s_waitcnt vmcnt(8)
	v_mov_b32_e32 v14, v134
	v_mov_b32_e32 v15, v135
	v_mov_b32_e32 v16, v136
	v_mov_b32_e32 v17, v137
	v_mov_b32_e32 v18, v138
	v_mov_b32_e32 v19, v139
	v_mov_b32_e32 v20, v140
	v_mov_b32_e32 v21, v141
	v_lshlrev_b32_e32 v13, 16, v14
	v_and_b32_e32 v14, 0xffff0000, v14
	v_fma_f32 v13, v13, v13, 0
	v_lshlrev_b32_e32 v22, 16, v15
	v_fmac_f32_e32 v13, v14, v14
	v_and_b32_e32 v15, 0xffff0000, v15
	v_fmac_f32_e32 v13, v22, v22
	v_lshlrev_b32_e32 v23, 16, v16
	v_fmac_f32_e32 v13, v15, v15
	v_lshlrev_b32_e32 v14, 16, v18
	v_and_b32_e32 v16, 0xffff0000, v16
	v_fmac_f32_e32 v13, v23, v23
	v_and_b32_e32 v15, 0xffff0000, v18
	v_fma_f32 v14, v14, v14, 0
	v_fmac_f32_e32 v13, v16, v16
	v_lshlrev_b32_e32 v16, 16, v19
	v_fmac_f32_e32 v14, v15, v15
	v_and_b32_e32 v18, 0xffff0000, v19
	v_fmac_f32_e32 v14, v16, v16
	v_lshlrev_b32_e32 v19, 16, v20
	v_fmac_f32_e32 v14, v18, v18
	v_and_b32_e32 v20, 0xffff0000, v20
	v_fmac_f32_e32 v14, v19, v19
	v_lshlrev_b32_e32 v24, 16, v17
	v_lshlrev_b32_e32 v22, 16, v21
	v_fmac_f32_e32 v14, v20, v20
	v_and_b32_e32 v17, 0xffff0000, v17
	v_and_b32_e32 v21, 0xffff0000, v21
	v_fmac_f32_e32 v13, v24, v24
	v_fmac_f32_e32 v14, v22, v22
	v_fmac_f32_e32 v13, v17, v17
	v_fmac_f32_e32 v14, v21, v21
	ds_bpermute_b32 v15, v8, v13
	ds_bpermute_b32 v16, v8, v14
	s_waitcnt lgkmcnt(1)
	v_add_f32_e32 v13, v13, v15
	s_waitcnt lgkmcnt(0)
	v_add_f32_e32 v14, v14, v16
	ds_bpermute_b32 v15, v9, v13
	ds_bpermute_b32 v16, v9, v14
	s_waitcnt lgkmcnt(1)
	v_add_f32_e32 v13, v13, v15
	s_waitcnt lgkmcnt(0)
	v_add_f32_e32 v14, v14, v16
	ds_bpermute_b32 v15, v10, v13
	ds_bpermute_b32 v16, v10, v14
	s_waitcnt lgkmcnt(1)
	v_add_f32_e32 v13, v13, v15
	s_waitcnt lgkmcnt(0)
; template <int PH>
; __device__ __forceinline__ void mk_body(const Args& a) {
;     ...
;                 const u32x4 v = *(const u32x4*)(y0 + (size_t)(blk * 32 + i) * Y0P + Y0_FK + 8 * lane);
;                 float s = 0.f;
; #pragma unroll
;                 for (int j = 0; j < 4; ++j) { const float lo_ = __uint_as_float(v[j] << 16), hi_ = __uint_as_float(v[j] & 0xffff0000u); s = fmaf(lo_, lo_, s); s = fmaf(hi_, hi_, s); }
;                 s += __shfl_xor(s, 1); s += __shfl_xor(s, 2); s += __shfl_xor(s, 4);
;                 mx2 = fmaxf(mx2, s);
	v_add_f32_e32 v14, v14, v16
	v_max3_f32 v12, v12, v13, v14
	s_waitcnt vmcnt(6)
	v_mov_b32_e32 v14, v142
	v_mov_b32_e32 v15, v143
	v_mov_b32_e32 v16, v144
	v_mov_b32_e32 v17, v145
	v_mov_b32_e32 v18, v146
	v_mov_b32_e32 v19, v147
	v_mov_b32_e32 v20, v148
	v_mov_b32_e32 v21, v149
	v_lshlrev_b32_e32 v13, 16, v14
	v_and_b32_e32 v14, 0xffff0000, v14
	v_fma_f32 v13, v13, v13, 0
	v_lshlrev_b32_e32 v22, 16, v15
	v_fmac_f32_e32 v13, v14, v14
	v_and_b32_e32 v15, 0xffff0000, v15
	v_fmac_f32_e32 v13, v22, v22
	v_lshlrev_b32_e32 v23, 16, v16
	v_fmac_f32_e32 v13, v15, v15
	v_lshlrev_b32_e32 v14, 16, v18
	v_and_b32_e32 v16, 0xffff0000, v16
	v_fmac_f32_e32 v13, v23, v23
	v_and_b32_e32 v15, 0xffff0000, v18
	v_fma_f32 v14, v14, v14, 0
	v_fmac_f32_e32 v13, v16, v16
	v_lshlrev_b32_e32 v16, 16, v19
	v_fmac_f32_e32 v14, v15, v15
	v_and_b32_e32 v18, 0xffff0000, v19
	v_fmac_f32_e32 v14, v16, v16
	v_lshlrev_b32_e32 v19, 16, v20
	v_fmac_f32_e32 v14, v18, v18
	v_and_b32_e32 v20, 0xffff0000, v20
	v_fmac_f32_e32 v14, v19, v19
	v_lshlrev_b32_e32 v24, 16, v17
	v_lshlrev_b32_e32 v22, 16, v21
	v_fmac_f32_e32 v14, v20, v20
	v_and_b32_e32 v17, 0xffff0000, v17
	v_and_b32_e32 v21, 0xffff0000, v21
	v_fmac_f32_e32 v13, v24, v24
	v_fmac_f32_e32 v14, v22, v22
	v_fmac_f32_e32 v13, v17, v17
	v_fmac_f32_e32 v14, v21, v21
	ds_bpermute_b32 v15, v8, v13
	ds_bpermute_b32 v16, v8, v14
	s_waitcnt lgkmcnt(1)
	v_add_f32_e32 v13, v13, v15
	s_waitcnt lgkmcnt(0)
	v_add_f32_e32 v14, v14, v16
	ds_bpermute_b32 v15, v9, v13
	ds_bpermute_b32 v16, v9, v14
	s_waitcnt lgkmcnt(1)
	v_add_f32_e32 v13, v13, v15
	s_waitcnt lgkmcnt(0)
	v_add_f32_e32 v14, v14, v16
	ds_bpermute_b32 v15, v10, v13
	ds_bpermute_b32 v16, v10, v14
	s_waitcnt lgkmcnt(1)
	v_add_f32_e32 v13, v13, v15
	s_waitcnt lgkmcnt(0)
	v_add_f32_e32 v14, v14, v16
	v_max3_f32 v12, v12, v13, v14
	s_waitcnt vmcnt(4)
	v_mov_b32_e32 v14, v150
	v_mov_b32_e32 v15, v151
	v_mov_b32_e32 v16, v152
	v_mov_b32_e32 v17, v153
	v_mov_b32_e32 v18, v154
	v_mov_b32_e32 v19, v155
	v_mov_b32_e32 v20, v156
	v_mov_b32_e32 v21, v157
	v_lshlrev_b32_e32 v13, 16, v14
	v_and_b32_e32 v14, 0xffff0000, v14
	v_fma_f32 v13, v13, v13, 0
	v_lshlrev_b32_e32 v22, 16, v15
	v_fmac_f32_e32 v13, v14, v14
	v_and_b32_e32 v15, 0xffff0000, v15
	v_fmac_f32_e32 v13, v22, v22
	v_lshlrev_b32_e32 v23, 16, v16
	v_fmac_f32_e32 v13, v15, v15
	v_lshlrev_b32_e32 v14, 16, v18
	v_and_b32_e32 v16, 0xffff0000, v16
	v_fmac_f32_e32 v13, v23, v23
	v_and_b32_e32 v15, 0xffff0000, v18
	v_fma_f32 v14, v14, v14, 0
	v_fmac_f32_e32 v13, v16, v16
	v_lshlrev_b32_e32 v16, 16, v19
	v_fmac_f32_e32 v14, v15, v15
	v_and_b32_e32 v18, 0xffff0000, v19
	v_fmac_f32_e32 v14, v16, v16
	v_lshlrev_b32_e32 v19, 16, v20
	v_fmac_f32_e32 v14, v18, v18
	v_and_b32_e32 v20, 0xffff0000, v20
	v_fmac_f32_e32 v14, v19, v19
	v_lshlrev_b32_e32 v24, 16, v17
	v_lshlrev_b32_e32 v22, 16, v21
	v_fmac_f32_e32 v14, v20, v20
	v_and_b32_e32 v17, 0xffff0000, v17
	v_and_b32_e32 v21, 0xffff0000, v21
	v_fmac_f32_e32 v13, v24, v24
	v_fmac_f32_e32 v14, v22, v22
	v_fmac_f32_e32 v13, v17, v17
	v_fmac_f32_e32 v14, v21, v21
	ds_bpermute_b32 v15, v8, v13
	ds_bpermute_b32 v16, v8, v14
	s_waitcnt lgkmcnt(1)
	v_add_f32_e32 v13, v13, v15
	s_waitcnt lgkmcnt(0)
	v_add_f32_e32 v14, v14, v16
	ds_bpermute_b32 v15, v9, v13
	ds_bpermute_b32 v16, v9, v14
	s_waitcnt lgkmcnt(1)
	v_add_f32_e32 v13, v13, v15
	s_waitcnt lgkmcnt(0)
	v_add_f32_e32 v14, v14, v16
	ds_bpermute_b32 v15, v10, v13
	ds_bpermute_b32 v16, v10, v14
	s_waitcnt lgkmcnt(1)
	v_add_f32_e32 v13, v13, v15
	s_waitcnt lgkmcnt(0)
	v_add_f32_e32 v14, v14, v16
	v_max3_f32 v12, v12, v13, v14
	s_waitcnt vmcnt(2)
; template <int PH>
; __device__ __forceinline__ void mk_body(const Args& a) {
;     ...
;                 const u32x4 v = *(const u32x4*)(y0 + (size_t)(blk * 32 + i) * Y0P + Y0_FK + 8 * lane);
;                 float s = 0.f;
; #pragma unroll
;                 for (int j = 0; j < 4; ++j) { const float lo_ = __uint_as_float(v[j] << 16), hi_ = __uint_as_float(v[j] & 0xffff0000u); s = fmaf(lo_, lo_, s); s = fmaf(hi_, hi_, s); }
;                 s += __shfl_xor(s, 1); s += __shfl_xor(s, 2); s += __shfl_xor(s, 4);
;                 mx2 = fmaxf(mx2, s);
;             }
;             if ((lane & 7) == 0) atomicMax(ctl + CW_KMAX + ((blk * 32) / S) * 8 + (lane >> 3), __float_as_uint(mx2));
	v_mov_b32_e32 v14, v158
	v_mov_b32_e32 v15, v159
	v_mov_b32_e32 v16, v160
	v_mov_b32_e32 v17, v161
	v_mov_b32_e32 v18, v162
	v_mov_b32_e32 v19, v163
	v_mov_b32_e32 v20, v164
	v_mov_b32_e32 v21, v165
	v_lshlrev_b32_e32 v13, 16, v14
	v_and_b32_e32 v14, 0xffff0000, v14
	v_fma_f32 v13, v13, v13, 0
	v_lshlrev_b32_e32 v22, 16, v15
	v_fmac_f32_e32 v13, v14, v14
	v_and_b32_e32 v15, 0xffff0000, v15
	v_fmac_f32_e32 v13, v22, v22
	v_lshlrev_b32_e32 v23, 16, v16
	v_fmac_f32_e32 v13, v15, v15
	v_lshlrev_b32_e32 v14, 16, v18
	v_and_b32_e32 v16, 0xffff0000, v16
	v_fmac_f32_e32 v13, v23, v23
	v_and_b32_e32 v15, 0xffff0000, v18
	v_fma_f32 v14, v14, v14, 0
	v_fmac_f32_e32 v13, v16, v16
	v_lshlrev_b32_e32 v16, 16, v19
	v_fmac_f32_e32 v14, v15, v15
	v_and_b32_e32 v18, 0xffff0000, v19
	v_fmac_f32_e32 v14, v16, v16
	v_lshlrev_b32_e32 v19, 16, v20
	v_fmac_f32_e32 v14, v18, v18
	v_and_b32_e32 v20, 0xffff0000, v20
	v_fmac_f32_e32 v14, v19, v19
	v_lshlrev_b32_e32 v24, 16, v17
	v_lshlrev_b32_e32 v22, 16, v21
	v_fmac_f32_e32 v14, v20, v20
	v_and_b32_e32 v17, 0xffff0000, v17
	v_and_b32_e32 v21, 0xffff0000, v21
	v_fmac_f32_e32 v13, v24, v24
	v_fmac_f32_e32 v14, v22, v22
	v_fmac_f32_e32 v13, v17, v17
	v_fmac_f32_e32 v14, v21, v21
	ds_bpermute_b32 v15, v8, v13
	ds_bpermute_b32 v16, v8, v14
	s_waitcnt lgkmcnt(1)
	v_add_f32_e32 v13, v13, v15
	s_waitcnt lgkmcnt(0)
	v_add_f32_e32 v14, v14, v16
	ds_bpermute_b32 v15, v9, v13
	ds_bpermute_b32 v16, v9, v14
	s_waitcnt lgkmcnt(1)
	v_add_f32_e32 v13, v13, v15
	s_waitcnt lgkmcnt(0)
	v_add_f32_e32 v14, v14, v16
	ds_bpermute_b32 v15, v10, v13
	ds_bpermute_b32 v16, v10, v14
	s_waitcnt lgkmcnt(1)
	v_add_f32_e32 v13, v13, v15
	s_waitcnt lgkmcnt(0)
	v_add_f32_e32 v14, v14, v16
	v_max3_f32 v12, v12, v13, v14
	s_waitcnt vmcnt(0)
	v_mov_b32_e32 v14, v166
	v_mov_b32_e32 v15, v167
	v_mov_b32_e32 v16, v168
	v_mov_b32_e32 v17, v169
	v_mov_b32_e32 v18, v170
	v_mov_b32_e32 v19, v171
	v_mov_b32_e32 v20, v172
	v_mov_b32_e32 v21, v173
	v_lshlrev_b32_e32 v13, 16, v14
	v_and_b32_e32 v14, 0xffff0000, v14
	v_fma_f32 v13, v13, v13, 0
	v_lshlrev_b32_e32 v22, 16, v15
	v_fmac_f32_e32 v13, v14, v14
	v_and_b32_e32 v15, 0xffff0000, v15
	v_fmac_f32_e32 v13, v22, v22
	v_lshlrev_b32_e32 v23, 16, v16
	v_fmac_f32_e32 v13, v15, v15
	v_lshlrev_b32_e32 v14, 16, v18
	v_and_b32_e32 v16, 0xffff0000, v16
	v_fmac_f32_e32 v13, v23, v23
	v_and_b32_e32 v15, 0xffff0000, v18
	v_fma_f32 v14, v14, v14, 0
	v_fmac_f32_e32 v13, v16, v16
	v_lshlrev_b32_e32 v16, 16, v19
	v_fmac_f32_e32 v14, v15, v15
	v_and_b32_e32 v18, 0xffff0000, v19
	v_fmac_f32_e32 v14, v16, v16
	v_lshlrev_b32_e32 v19, 16, v20
	v_fmac_f32_e32 v14, v18, v18
	v_and_b32_e32 v20, 0xffff0000, v20
	v_fmac_f32_e32 v14, v19, v19
	v_lshlrev_b32_e32 v24, 16, v17
	v_lshlrev_b32_e32 v22, 16, v21
	v_fmac_f32_e32 v14, v20, v20
	v_and_b32_e32 v17, 0xffff0000, v17
	v_and_b32_e32 v21, 0xffff0000, v21
	v_fmac_f32_e32 v13, v24, v24
	v_fmac_f32_e32 v14, v22, v22
	v_fmac_f32_e32 v13, v17, v17
	v_fmac_f32_e32 v14, v21, v21
	ds_bpermute_b32 v15, v8, v13
	ds_bpermute_b32 v16, v8, v14
	s_waitcnt lgkmcnt(1)
	v_add_f32_e32 v13, v13, v15
	s_waitcnt lgkmcnt(0)
	v_add_f32_e32 v14, v14, v16
	ds_bpermute_b32 v15, v9, v13
	ds_bpermute_b32 v16, v9, v14
	s_waitcnt lgkmcnt(1)
	v_add_f32_e32 v13, v13, v15
	s_waitcnt lgkmcnt(0)
	v_add_f32_e32 v14, v14, v16
	ds_bpermute_b32 v15, v10, v13
	ds_bpermute_b32 v16, v10, v14
	s_waitcnt lgkmcnt(1)
	v_add_f32_e32 v13, v13, v15
	s_waitcnt lgkmcnt(0)
	v_add_f32_e32 v14, v14, v16
	v_max3_f32 v12, v12, v13, v14
	s_and_saveexec_b64 s[2:3], vcc
	s_cbranch_execz .LBB0_554
	s_ashr_i32 s9, s8, 31
	s_lshr_b32 s9, s9, 24
	s_add_i32 s9, s8, s9
	s_ashr_i32 s9, s9, 8
	s_lshl_b32 s10, s9, 3
	s_ashr_i32 s11, s10, 31
	v_lshl_add_u64 v[6:7], s[10:11], 2, v[2:3]
	global_atomic_umax v[6:7], v12, off
	s_branch .LBB0_554
